# phase 13 S5 readout: item bits permuted so that an XCD owns the 4 groups g that share a 128-byte line of each token row
# speedup vs baseline: 1.0156x; 1.0049x over previous
; __device__ __forceinline__ void phase_s5c(const Params& P, unsigned char* smraw, int bid, int nb) {
;     const bfr* QK = (const bfr*)(P.ws + WS_QKVU);
;     const float* CINF = (const float*)(P.ws + WS_CIN);
;     const bfr* S5F = (const bfr*)(P.ws + WS_S5F);
;     const bfr* S5G = (const bfr*)(P.ws + WS_S5G);
;     const float* dsk = P.in[33];
;     bfr* Y5 = (bfr*)(P.ws + WS_Y5);
;     const int tid = threadIdx.x, lane = tid & 63, wave = tid >> 6;
;     bfr* Us = (bfr*)smraw;
;     bfr* Fs = (bfr*)(smraw + 65536);
;     for (int item = bid; item < 256; item += nb) {
;         const int g = item & 31, nt8 = item >> 5;
;         __syncthreads();
;         for (int e = tid; e < 4096; e += NTHR) {
;             const int tl = e >> 6, l = e & 63;
;             const int row = NCTX + (nt8 * 32 + (l & 31)) * 64 + tl;
;             *(u32x4*)&Us[(size_t)e * 8] = *(const u32x4*)(QK + (size_t)row * 1280 + 768 + g * 16 + (l >> 5) * 8);
.LBB0_1950:
	s_cmp_lt_i32 s6, 14
	s_cselect_b64 s[0:1], -1, 0
	s_cmp_gt_i32 s7, 13
	s_cselect_b64 s[2:3], -1, 0
	s_and_b64 s[0:1], s[0:1], s[2:3]
	s_andn2_b64 vcc, exec, s[0:1]
	s_cbranch_vccnz .LBB0_2056
	s_cmpk_gt_i32 s44, 0xff
	s_cbranch_scc1 .LBB0_2002
	v_readlane_b32 s0, v252, 19
	v_readlane_b32 s2, v252, 21
	v_readlane_b32 s3, v252, 22
	s_add_u32 s20, s2, 0x41766400
	s_addc_u32 s21, s3, 0
	s_waitcnt lgkmcnt(1)
	v_lshlrev_b32_e32 v3, 4, v0
	s_add_u32 s22, s2, 0x3b152400
	v_and_b32_e32 v2, 0x3f0, v3
	v_readlane_b32 s1, v252, 20
	s_addc_u32 s23, s3, 0
	s_waitcnt vmcnt(2)
	v_add_u32_e32 v75, 0, v2
	v_lshrrev_b32_e32 v2, 3, v0
	s_add_i32 s0, 0, 0x10010
	v_lshrrev_b32_e32 v1, 6, v0
	v_and_b32_e32 v77, 31, v0
	v_and_b32_e32 v76, 4, v2
	s_movk_i32 s1, 0x804
	v_mov_b32_e32 v2, s0
	v_lshlrev_b32_e32 v81, 1, v1
	v_mad_u32_u24 v2, v77, s1, v2
	v_lshlrev_b32_e32 v10, 1, v76
	v_and_b32_e32 v11, 0x1c0, v0
	s_waitcnt vmcnt(1)
	v_add3_u32 v86, v2, v11, v10
	v_or_b32_e32 v11, 1, v81
	v_or_b32_e32 v4, 16, v81
	v_lshl_add_u32 v12, v11, 10, 0
	v_lshlrev_b32_e32 v11, 5, v11
	v_add3_u32 v88, v2, v11, v10
	v_lshl_add_u32 v11, v4, 10, 0
	v_lshlrev_b32_e32 v4, 5, v4
	v_lshlrev_b32_e32 v9, 4, v77
	v_add3_u32 v90, v2, v4, v10
	v_or_b32_e32 v4, 17, v81
	v_or_b32_e32 v6, 32, v81
	v_add3_u32 v89, v11, v9, v10
	v_lshl_add_u32 v11, v4, 10, 0
	v_lshlrev_b32_e32 v4, 5, v4
	v_add3_u32 v92, v2, v4, v10
	v_lshl_add_u32 v4, v6, 10, 0
	v_add3_u32 v93, v4, v9, v10
	v_lshlrev_b32_e32 v4, 5, v6
	v_add3_u32 v94, v2, v4, v10
	v_or_b32_e32 v4, 33, v81
	v_or_b32_e32 v7, 48, v81
	v_lshl_add_u32 v6, v4, 10, 0
	v_lshlrev_b32_e32 v4, 5, v4
	v_add3_u32 v96, v2, v4, v10
	v_lshl_add_u32 v4, v7, 10, 0
	v_add3_u32 v97, v4, v9, v10
	v_lshlrev_b32_e32 v4, 5, v7
	v_add3_u32 v98, v2, v4, v10
	v_or_b32_e32 v4, 49, v81
	v_lshlrev_b32_e32 v74, 3, v0
	v_add3_u32 v95, v6, v9, v10
	v_lshl_add_u32 v6, v4, 10, 0
	v_lshlrev_b32_e32 v4, 5, v4
	s_waitcnt lgkmcnt(0)
	v_bfe_u32 v5, v0, 1, 6
	v_add3_u32 v100, v2, v4, v10
	v_or_b32_e32 v2, 0x2000, v74
	v_or_b32_e32 v4, 0x4000, v74
	v_or_b32_e32 v7, 0xc00, v0
	v_lshlrev_b32_e32 v8, 11, v1
	v_lshl_add_u32 v101, v5, 5, s0
	v_add_u32_e32 v102, s0, v3
	v_lshl_add_u32 v104, v2, 1, s0
	v_lshl_add_u32 v106, v4, 1, s0
	v_lshl_add_u32 v108, v7, 4, s0
	s_movk_i32 s0, 0xe00
	v_add3_u32 v111, v3, 0, 16
	v_lshl_or_b32 v3, v77, 6, v1
	v_mov_b32_e32 v79, 0
	v_add_u32_e32 v84, 0, v8
	v_add3_u32 v99, v6, v9, v10
	v_lshlrev_b32_e32 v6, 3, v7
	v_cmp_gt_u32_e64 s[4:5], s0, v7
	v_add_u32_e32 v113, 0x100, v3
	v_lshlrev_b32_e32 v114, 4, v202
	v_mov_b32_e32 v3, 0x3b14e440
	v_lshrrev_b32_e32 v118, 7, v0
	v_readlane_b32 s0, v252, 23
	s_mov_b32 s3, 0
	s_mov_b32 s24, 0x10010
	v_add3_u32 v85, v84, v9, v10
	v_add3_u32 v87, v12, v9, v10
	v_add3_u32 v91, v11, v9, v10
	s_movk_i32 s25, 0x2000
	v_add_u32_e32 v103, 0x2000, v102
	s_movk_i32 s26, 0x6000
	v_add_u32_e32 v105, 0x6000, v102
	v_add_u32_e32 v107, 0xa000, v102
	v_add_u32_e32 v109, 0xe000, v102
	v_or_b32_e32 v110, 0xfffffe00, v0
	v_lshrrev_b32_e32 v112, 2, v0
	v_add_u32_e32 v115, 4, v77
	v_lshl_or_b32 v80, v1, 13, v114
	v_mov_b32_e32 v1, v79
	v_sub_u32_e32 v116, 0, v8
	v_sub_u32_e32 v117, 0, v81
	v_and_or_b32 v82, v0, 32, v3
	v_mov_b32_e32 v83, v79
	v_lshl_or_b32 v119, v118, 6, v5
	s_movk_i32 s27, 0xa00
	s_movk_i32 s28, 0xdff
	v_lshlrev_b32_e32 v120, 1, v2
	v_lshlrev_b32_e32 v121, 1, v4
	v_lshlrev_b32_e32 v122, 1, v6
	s_mov_b32 s29, 0x10410
	s_mov_b32 s30, 0x14410
	s_mov_b32 s31, 0x18410
	s_mov_b32 s34, 0x1c410
	s_mov_b32 s35, 0x14010
	s_mov_b32 s36, 0x18010
	s_mov_b32 s37, 0x1c010
	s_mov_b64 s[10:11], 0x3a932400
	s_mov_b32 s38, 0x41b66000
	s_mov_b32 s39, 0x41b76000
	s_mov_b32 s40, 0x41b86000
	s_mov_b32 s41, 0x41b96000
	s_mov_b64 s[12:13], 0x3a932440
	s_mov_b64 s[14:15], 0x80
	s_mov_b64 s[16:17], 0x800
	s_mov_b32 s42, 0x42366000
	s_mov_b32 s43, 0x42376000
	s_mov_b32 s44, 0x42386000
	s_mov_b32 s45, 0x42396000
	s_mov_b32 s46, s0
	s_mov_b32 s47, s0
	v_readlane_b32 s96, v253, 10
	s_cmpk_lg_u32 s96, 0x100
	s_cbranch_scc1 .Ls5c_xcd
	s_and_b32 s47, s0, 0xe0
	s_and_b32 s97, s0, 7
	s_lshl_b32 s97, s97, 2
	s_or_b32 s47, s47, s97
	s_bfe_u32 s97, s0, 0x20003
	s_or_b32 s47, s47, s97
	s_mov_b32 s46, s47
.Ls5c_xcd:
	v_readlane_b32 s1, v252, 24
